# speedup vs baseline: 1.0098x; 1.0098x over previous
.LBB0_6:
	s_or_b64 exec, exec, s[6:7]
	s_waitcnt lgkmcnt(0)
	v_lshl_add_u64 v[6:7], v[6:7], 1, s[4:5]
	global_store_dwordx4 v[6:7], v[2:5], off sc0 sc1
	s_mov_b64 s[4:5], 0
.LBB0_7:
	s_and_b64 vcc, exec, s[4:5]
	s_cbranch_vccz .LBB0_9
	s_load_dwordx8 s[4:11], s[0:1], 0x8
	s_lshl_b32 s13, s2, 2
	s_add_i32 s3, s2, 0xfffffe00
	s_and_b32 s14, s13, 0x3c0
	s_lshl_b32 s13, s2, 6
	s_lshr_b32 s12, s3, 8
	s_and_b32 s15, s13, 0x3c0
	s_cmp_eq_u32 s12, 2
	s_waitcnt lgkmcnt(0)
	s_cselect_b32 s9, s9, s11
	s_cselect_b32 s8, s8, s10
	s_cmp_eq_u32 s12, 1
	s_cselect_b32 s6, s6, s8
	s_cselect_b32 s7, s7, s9
	s_cmpk_lt_u32 s3, 0x100
	s_mov_b32 s13, 0
	s_cselect_b32 s3, s5, s7
	s_cselect_b32 s6, s4, s6
	s_lshl_b64 s[4:5], s[12:13], 21
	v_lshlrev_b32_e32 v2, 2, v0
	s_lshl_b32 s7, s15, 2
	v_lshrrev_b32_e32 v1, 4, v0
	v_and_b32_e32 v20, 60, v2
	s_add_u32 s6, s6, s7
	s_addc_u32 s7, s3, 0
	v_lshlrev_b32_e32 v18, 2, v20
	v_mov_b32_e32 v19, 0
	v_or_b32_e32 v2, s14, v1
	v_lshl_add_u64 v[14:15], s[6:7], 0, v[18:19]
	v_lshlrev_b32_e32 v18, 12, v2
	v_lshl_add_u64 v[2:3], v[14:15], 0, v[18:19]
	global_load_dwordx4 v[2:5], v[2:3], off nt
	v_or_b32_e32 v6, 0x10000, v18
	v_mov_b32_e32 v7, v19
	v_lshl_add_u64 v[6:7], v[14:15], 0, v[6:7]
	v_or_b32_e32 v10, 0x20000, v18
	v_mov_b32_e32 v11, v19
	v_or_b32_e32 v18, 0x30000, v18
	global_load_dwordx4 v[6:9], v[6:7], off nt
	v_lshl_add_u64 v[10:11], v[14:15], 0, v[10:11]
	v_lshl_add_u64 v[14:15], v[14:15], 0, v[18:19]
	global_load_dwordx4 v[10:13], v[10:11], off nt
	s_load_dwordx2 s[6:7], s[0:1], 0x38
	global_load_dwordx4 v[14:17], v[14:15], off nt
	v_lshlrev_b32_e32 v18, 4, v0
	s_movk_i32 s3, 0x90
	v_lshrrev_b32_e32 v21, 3, v0
	v_mul_u32_u24_e32 v20, 0x90, v20
	v_and_b32_e32 v18, 0x70, v18
	v_lshl_or_b32 v1, v1, 1, v20
	s_waitcnt lgkmcnt(0)
	s_add_u32 s4, s6, s4
	v_mad_u32_u24 v23, v21, s3, v18
	s_addc_u32 s5, s7, s5
	s_lshl_b32 s6, s14, 1
	s_add_u32 s4, s4, s6
	v_or_b32_e32 v22, s15, v21
	s_addc_u32 s5, s5, 0
	v_lshl_add_u64 v[20:21], s[4:5], 0, v[18:19]
	v_lshlrev_b32_e32 v18, 11, v22
	s_waitcnt vmcnt(3)
	v_cvt_f16_f32_e32 v2, v2
	v_cvt_f16_f32_e32 v3, v3
	v_cvt_f16_f32_e32 v4, v4
	v_cvt_f16_f32_e32 v5, v5
	s_waitcnt vmcnt(2)
	v_cvt_f16_f32_e32 v6, v6
	v_cvt_f16_f32_e32 v7, v7
	v_cvt_f16_f32_e32 v8, v8
	v_cvt_f16_f32_e32 v9, v9
	s_waitcnt vmcnt(1)
	v_cvt_f16_f32_e32 v10, v10
	v_cvt_f16_f32_e32 v11, v11
	v_cvt_f16_f32_e32 v12, v12
	v_cvt_f16_f32_e32 v13, v13
	s_waitcnt vmcnt(0)
	v_cvt_f16_f32_e32 v14, v14
	v_cvt_f16_f32_e32 v15, v15
	v_cvt_f16_f32_e32 v16, v16
	v_cvt_f16_f32_e32 v17, v17
	ds_write_b16 v1, v2
	ds_write_b16 v1, v3 offset:144
	ds_write_b16 v1, v4 offset:288
	ds_write_b16 v1, v5 offset:432
	ds_write_b16 v1, v6 offset:32
	ds_write_b16 v1, v7 offset:176
	ds_write_b16 v1, v8 offset:320
	ds_write_b16 v1, v9 offset:464
	ds_write_b16 v1, v10 offset:64
	ds_write_b16 v1, v11 offset:208
	ds_write_b16 v1, v12 offset:352
	ds_write_b16 v1, v13 offset:496
	ds_write_b16 v1, v14 offset:96
	ds_write_b16 v1, v15 offset:240
	ds_write_b16 v1, v16 offset:384
	ds_write_b16 v1, v17 offset:528
	s_waitcnt lgkmcnt(0)
	s_barrier
	ds_read_b128 v[2:5], v23
	ds_read_b128 v[6:9], v23 offset:4608
	v_lshl_add_u64 v[10:11], v[20:21], 0, v[18:19]
	v_or_b32_e32 v18, 0x10000, v18
	v_lshl_add_u64 v[12:13], v[20:21], 0, v[18:19]
	s_waitcnt lgkmcnt(1)
	global_store_dwordx4 v[10:11], v[2:5], off sc0 sc1
	s_waitcnt lgkmcnt(0)
	global_store_dwordx4 v[12:13], v[6:9], off sc0 sc1

.LBB0_10:
	s_load_dwordx2 s[4:5], s[0:1], 0x0
	s_load_dwordx2 s[6:7], s[0:1], 0x30
	s_ashr_i32 s3, s2, 31
	s_lshl_b64 s[0:1], s[2:3], 13
	v_lshl_or_b32 v32, v0, 3, s0
	v_mov_b32_e32 v33, s1
	s_waitcnt lgkmcnt(0)
	v_lshl_add_u64 v[28:29], v[32:33], 2, s[4:5]
	v_add_co_u32_e32 v18, vcc, 0x2000, v28
	s_mov_b64 s[0:1], 0x2000
	s_nop 0
	v_addc_co_u32_e32 v19, vcc, 0, v29, vcc
	v_lshl_add_u64 v[16:17], v[28:29], 0, s[0:1]
	s_mov_b64 s[0:1], 0x4000
	v_add_co_u32_e32 v26, vcc, 0x4000, v28
	v_lshl_add_u64 v[24:25], v[28:29], 0, s[0:1]
	s_nop 0
	v_addc_co_u32_e32 v27, vcc, 0, v29, vcc
	global_load_dwordx4 v[0:3], v[28:29], off offset:16 nt
	global_load_dwordx4 v[4:7], v[28:29], off nt
	global_load_dwordx4 v[8:11], v[18:19], off nt
	global_load_dwordx4 v[12:15], v[16:17], off offset:16 nt
	s_nop 0
	global_load_dwordx4 v[16:19], v[26:27], off nt
	global_load_dwordx4 v[20:23], v[24:25], off offset:16 nt
	s_mov_b64 s[0:1], 0x6000
	v_add_co_u32_e32 v24, vcc, 0x6000, v28
	v_lshl_add_u64 v[32:33], v[32:33], 1, s[6:7]
	s_nop 0
	v_addc_co_u32_e32 v25, vcc, 0, v29, vcc
	v_lshl_add_u64 v[28:29], v[28:29], 0, s[0:1]
	global_load_dwordx4 v[24:27], v[24:25], off nt
	s_movk_i32 s0, 0x2000
	global_load_dwordx4 v[28:31], v[28:29], off offset:16 nt
	v_add_co_u32_e32 v34, vcc, s0, v32
	s_waitcnt vmcnt(6)
	v_cvt_pk_f16_f32 v4, v4, v5
	v_addc_co_u32_e32 v35, vcc, 0, v33, vcc
	v_cvt_pk_f16_f32 v5, v6, v7
	v_cvt_pk_f16_f32 v6, v0, v1
	v_cvt_pk_f16_f32 v7, v2, v3
	s_waitcnt vmcnt(5)
	v_cvt_pk_f16_f32 v0, v8, v9
	v_cvt_pk_f16_f32 v1, v10, v11
	s_waitcnt vmcnt(4)
	v_cvt_pk_f16_f32 v2, v12, v13
	v_cvt_pk_f16_f32 v3, v14, v15
	v_add_co_u32_e32 v36, vcc, 0x3000, v32
	global_store_dwordx4 v[34:35], v[0:3], off offset:-4096 sc0 sc1
	s_nop 0
	v_addc_co_u32_e32 v37, vcc, 0, v33, vcc
	s_waitcnt vmcnt(4)
	v_cvt_pk_f16_f32 v0, v16, v17
	v_cvt_pk_f16_f32 v1, v18, v19
	s_waitcnt vmcnt(3)
	v_cvt_pk_f16_f32 v2, v20, v21
	v_cvt_pk_f16_f32 v3, v22, v23
	global_store_dwordx4 v[34:35], v[0:3], off sc0 sc1
	global_store_dwordx4 v[32:33], v[4:7], off sc0 sc1
	s_waitcnt vmcnt(4)
	v_cvt_pk_f16_f32 v0, v24, v25
	v_cvt_pk_f16_f32 v1, v26, v27
	s_waitcnt vmcnt(3)
	v_cvt_pk_f16_f32 v2, v28, v29
	v_cvt_pk_f16_f32 v3, v30, v31
	global_store_dwordx4 v[36:37], v[0:3], off sc0 sc1
	s_endpgm
